# f26 plus removal of the unused first-touch tv load in the proj V variant (Q/K workgroups still perform that first touch)
# speedup vs baseline: 1.0081x; 1.0000x over previous
_Z11proj_kernelPKfS0_S0_S0_S0_S0_S0_S0_S0_S0_S0_S0_S0_PfS1_PDF16_S1_S0_S0_S2_:
	s_mov_b32 s88, s2
	s_load_dwordx2 s[16:17], s[0:1], 0x90
	s_load_dwordx4 s[4:7], s[0:1], 0x80
	s_cmpk_gt_u32 s2, 0x5f
	s_mov_b64 s[8:9], -1
	s_cbranch_scc0 .LBB0_16
	s_load_dwordx4 s[8:11], s[0:1], 0x58
	s_lshr_b32 s3, s2, 3
	s_cmpk_gt_u32 s2, 0xbf
	s_mov_b64 s[12:13], -1
	s_cbranch_scc0 .LBB0_3
	v_lshlrev_b32_e32 v54, 2, v0
	v_mov_b32_e32 v55, 0
	s_waitcnt lgkmcnt(0)
	v_lshl_add_u64 v[2:3], s[6:7], 0, v[54:55]
	v_lshl_add_u64 v[4:5], s[16:17], 0, v[54:55]
	v_cmp_gt_u32_e32 vcc, 64, v0
	s_load_dwordx4 s[12:15], s[0:1], 0x38
	s_load_dwordx2 s[22:23], s[0:1], 0x10
	v_cndmask_b32_e32 v2, v4, v2, vcc
	v_cndmask_b32_e32 v3, v5, v3, vcc
	v_lshrrev_b32_e32 v2, 2, v0
	v_and_b32_e32 v56, 15, v0
	v_and_b32_e32 v18, 48, v2
	v_or_b32_e32 v68, v18, v56
	v_bfe_u32 v1, v0, 4, 2
	v_lshlrev_b32_e32 v2, 8, v68
	v_mov_b32_e32 v3, v55
	s_lshl_b32 s20, s2, 1
	v_lshl_add_u64 v[2:3], s[8:9], 0, v[2:3]
	v_lshlrev_b32_e32 v4, 5, v1
	v_mov_b32_e32 v5, v55
	s_and_b32 s20, s20, 6
	s_bfe_u32 s21, s2, 0x10003
	v_lshl_add_u64 v[14:15], v[2:3], 0, v[4:5]
	s_sub_i32 s19, s3, 24
	s_or_b32 s21, s21, s20
	v_lshl_add_u64 v[6:7], v[14:15], 0, 16
	s_mov_b64 s[24:25], 0x80
	s_bfe_u32 s18, s2, 0x10002
	s_lshr_b32 s19, s19, 1
	s_lshl_b32 s20, s21, 6
	v_lshl_add_u64 v[10:11], v[14:15], 0, s[24:25]
	s_mov_b64 s[24:25], 0x90
	v_lshlrev_b32_e32 v22, 2, v18
	v_mov_b32_e32 v23, v55
	s_lshl_b32 s21, s21, 8
	v_lshl_add_u64 v[14:15], v[14:15], 0, s[24:25]
	v_lshl_add_u64 v[24:25], s[10:11], 0, v[22:23]
	v_lshlrev_b32_e32 v18, 4, v1
	v_mov_b32_e32 v19, v55
	s_waitcnt lgkmcnt(0)
	s_add_u32 s14, s14, s21
	v_lshl_add_u64 v[18:19], v[24:25], 0, v[18:19]
	s_addc_u32 s15, s15, 0
	v_lshlrev_b32_e32 v26, 2, v56
	v_mov_b32_e32 v27, v55
	v_lshl_add_u64 v[22:23], s[14:15], 0, v[22:23]
	s_mul_i32 s26, s18, 0x180
	v_lshrrev_b32_e32 v57, 4, v0
	v_lshl_add_u64 v[24:25], v[24:25], 0, v[26:27]
	v_lshl_add_u64 v[22:23], v[22:23], 0, v[26:27]
	s_mulk_i32 s19, 0x60
	global_load_dword v69, v[22:23], off
	v_or_b32_e32 v22, s26, v57
	v_add_u32_e32 v22, s19, v22
	v_mov_b32_e32 v23, v55
	v_lshlrev_b64 v[22:23], 11, v[22:23]
	v_and_b32_e32 v72, 60, v54
	v_lshl_add_u64 v[22:23], s[22:23], 0, v[22:23]
	v_lshlrev_b32_e32 v54, 2, v72
	v_lshl_add_u64 v[66:67], v[22:23], 0, v[54:55]
	global_load_dwordx4 v[22:25], v[66:67], off
	s_mov_b32 s14, 0x10000
	v_add_co_u32_e32 v64, vcc, s14, v66
	s_mov_b32 s15, 0x20000
	s_nop 0
	v_addc_co_u32_e32 v65, vcc, 0, v67, vcc
	global_load_dwordx4 v[30:33], v[64:65], off
	v_add_co_u32_e32 v62, vcc, s15, v66
	v_or_b32_e32 v26, s20, v57
	s_nop 0
	v_addc_co_u32_e32 v63, vcc, 0, v67, vcc
	global_load_dwordx4 v[34:37], v[62:63], off
	v_lshlrev_b32_e32 v26, 9, v26
	v_lshl_add_u64 v[26:27], v[26:27], 2, s[12:13]
	v_lshl_add_u64 v[60:61], v[26:27], 0, v[54:55]
	v_add_co_u32_e32 v58, vcc, s14, v60
	global_load_dwordx4 v[38:41], v[60:61], off
	s_nop 0
	v_addc_co_u32_e32 v59, vcc, 0, v61, vcc
	global_load_dwordx4 v[42:45], v[58:59], off
	global_load_dwordx4 v[46:49], v[66:67], off offset:256
	global_load_dwordx4 v[50:53], v[64:65], off offset:256
	global_load_dwordx4 v[74:77], v[62:63], off offset:256
	global_load_dwordx4 v[78:81], v[60:61], off offset:256
	global_load_dwordx4 v[82:85], v[58:59], off offset:256
	global_load_dwordx4 v[86:89], v[66:67], off offset:512
	global_load_dwordx4 v[90:93], v[64:65], off offset:512
	v_lshrrev_b32_e32 v26, 8, v0
	v_mul_u32_u24_e32 v54, 48, v26
	global_load_dwordx4 v[26:29], v[62:63], off offset:512
	global_load_dwordx4 v[94:97], v[60:61], off offset:512
	v_or_b32_e32 v102, v54, v56
	v_and_b32_e32 v56, 48, v0
	s_movk_i32 s14, 0xa0
	v_mad_u32_u24 v73, v68, s14, v56
	v_lshl_or_b32 v1, v1, 2, v54
	v_mul_lo_u32 v1, v1, s14
	v_lshl_add_u32 v1, v68, 1, v1
	s_movk_i32 s15, 0x180
	s_waitcnt vmcnt(13)
	v_cvt_f16_f32_e32 v22, v22
	v_cvt_f16_f32_e32 v25, v25
	v_cvt_pk_f16_f32 v23, v23, v24
	v_mul_u32_u24_e32 v24, 0xa0, v57
	v_pack_b32_f16 v22, v22, v23
	v_alignbit_b32 v23, v25, v23, 16
	v_lshl_add_u32 v72, v72, 1, v24
	s_waitcnt vmcnt(12)
	v_cvt_f16_f32_e32 v25, v30
	v_cvt_f16_f32_e32 v30, v33
	v_cvt_pk_f16_f32 v31, v31, v32
	v_mad_u64_u32 v[56:57], s[12:13], v102, s14, v[56:57]
	v_pack_b32_f16 v24, v25, v31
	v_alignbit_b32 v25, v30, v31, 16
	s_waitcnt vmcnt(11)
	v_cvt_f16_f32_e32 v30, v34
	ds_write2st64_b64 v72, v[22:23], v[24:25] offset1:10
	s_waitcnt vmcnt(8)
	v_cvt_f16_f32_e32 v34, v46
	v_cvt_pk_f16_f32 v23, v35, v36
	v_cvt_f16_f32_e32 v35, v49
	v_cvt_pk_f16_f32 v36, v47, v48
	v_pack_b32_f16 v102, v34, v36
	s_waitcnt vmcnt(7)
	v_cvt_f16_f32_e32 v34, v50
	v_alignbit_b32 v103, v35, v36, 16
	v_cvt_f16_f32_e32 v35, v53
	v_cvt_pk_f16_f32 v36, v51, v52
	v_pack_b32_f16 v104, v34, v36
	s_waitcnt vmcnt(6)
	v_cvt_f16_f32_e32 v34, v74
	v_alignbit_b32 v105, v35, v36, 16
	v_cvt_f16_f32_e32 v35, v77
	v_cvt_pk_f16_f32 v36, v75, v76
	v_pack_b32_f16 v106, v34, v36
	s_waitcnt vmcnt(5)
	v_cvt_f16_f32_e32 v34, v78
	v_alignbit_b32 v107, v35, v36, 16
	v_cvt_f16_f32_e32 v35, v81
	v_cvt_pk_f16_f32 v36, v79, v80
	v_pack_b32_f16 v108, v34, v36
	s_waitcnt vmcnt(4)
	v_cvt_f16_f32_e32 v34, v82
	v_cvt_f16_f32_e32 v24, v37
	v_pack_b32_f16 v22, v30, v23
	v_cvt_f16_f32_e32 v25, v38
	v_cvt_f16_f32_e32 v30, v41
	v_alignbit_b32 v109, v35, v36, 16
	v_cvt_f16_f32_e32 v35, v85
	v_cvt_pk_f16_f32 v36, v83, v84
	v_cvt_pk_f16_f32 v31, v39, v40
	v_pack_b32_f16 v110, v34, v36
	s_waitcnt vmcnt(3)
	v_cvt_f16_f32_e32 v34, v86
	v_alignbit_b32 v23, v24, v23, 16
	v_pack_b32_f16 v24, v25, v31
	v_alignbit_b32 v25, v30, v31, 16
	v_cvt_f16_f32_e32 v30, v42
	v_cvt_f16_f32_e32 v31, v45
	v_alignbit_b32 v111, v35, v36, 16
	v_cvt_pk_f16_f32 v36, v87, v88
	v_cvt_pk_f16_f32 v32, v43, v44
	v_cvt_f16_f32_e32 v35, v89
	v_pack_b32_f16 v114, v34, v36
	s_waitcnt vmcnt(2)
	v_cvt_f16_f32_e32 v34, v90
	v_pack_b32_f16 v30, v30, v32
	v_alignbit_b32 v31, v31, v32, 16
	ds_write2st64_b64 v72, v[22:23], v[24:25] offset0:20 offset1:60
	global_load_dwordx4 v[22:25], v[58:59], off offset:512
	ds_write_b64 v72, v[30:31] offset:35840
	s_waitcnt lgkmcnt(0)
	s_barrier
	global_load_dwordx4 v[30:33], v[66:67], off offset:768
	global_load_dwordx4 v[98:101], v[64:65], off offset:768
	v_cvt_pk_f16_f32 v39, v91, v92
	v_alignbit_b32 v115, v35, v36, 16
	v_cvt_f16_f32_e32 v38, v93
	v_pack_b32_f16 v116, v34, v39
	ds_read_b128 v[34:37], v56
	s_waitcnt vmcnt(4)
	v_cvt_f16_f32_e32 v57, v26
	v_alignbit_b32 v117, v38, v39, 16
	ds_read_b128 v[38:41], v56 offset:2560
	ds_read_b128 v[46:49], v73 offset:30720
	ds_read_b128 v[50:53], v56 offset:5120
	ds_read_b128 v[74:77], v56 offset:64
	ds_read_b128 v[78:81], v73 offset:30784
	v_cvt_f16_f32_e32 v87, v29
	s_waitcnt lgkmcnt(3)
	v_mfma_f32_16x16x32_f16 v[34:37], v[34:37], v[46:49], 0
	v_cvt_pk_f16_f32 v86, v27, v28
	global_load_dwordx4 v[42:45], v[62:63], off offset:768
	ds_read_b128 v[26:29], v56 offset:2624
	v_mfma_f32_16x16x32_f16 v[82:85], v[38:41], v[46:49], 0
	v_pack_b32_f16 v118, v57, v86
	v_alignbit_b32 v119, v87, v86, 16
	ds_read_b128 v[86:89], v56 offset:5184
	s_waitcnt lgkmcnt(4)
	v_mfma_f32_16x16x32_f16 v[50:53], v[50:53], v[46:49], 0
	global_load_dwordx4 v[46:49], v[60:61], off offset:768
	ds_write2st64_b64 v72, v[102:103], v[104:105] offset0:30 offset1:40
	ds_write2st64_b64 v72, v[106:107], v[108:109] offset0:50 offset1:80
	ds_write_b64 v72, v[110:111] offset:46080
	s_waitcnt lgkmcnt(5)
	v_mfma_f32_16x16x32_f16 v[74:77], v[74:77], v[78:81], v[34:37]
	s_waitcnt vmcnt(5)
	v_cvt_f16_f32_e32 v57, v94
	v_cvt_f16_f32_e32 v90, v97
	v_cvt_pk_f16_f32 v91, v95, v96
	global_load_dwordx4 v[34:37], v[58:59], off offset:768
	s_waitcnt lgkmcnt(0)
	s_barrier
	global_load_dwordx4 v[38:41], v[66:67], off offset:1024
	v_pack_b32_f16 v120, v57, v91
	v_alignbit_b32 v121, v90, v91, 16
	global_load_dwordx4 v[90:93], v[64:65], off offset:1024
	v_mfma_f32_16x16x32_f16 v[50:53], v[86:89], v[78:81], v[50:53]
	global_load_dwordx4 v[86:89], v[62:63], off offset:1024
	s_load_dwordx2 s[12:13], s[0:1], 0x78
	s_waitcnt vmcnt(8)
	v_cvt_f16_f32_e32 v22, v22
	v_mfma_f32_16x16x32_f16 v[82:85], v[26:29], v[78:81], v[82:85]
	v_cvt_f16_f32_e32 v25, v25
	v_cvt_pk_f16_f32 v23, v23, v24
	v_pack_b32_f16 v122, v22, v23
	s_waitcnt vmcnt(7)
	v_cvt_f16_f32_e32 v26, v30
	v_cvt_pk_f16_f32 v57, v31, v32
	v_alignbit_b32 v123, v25, v23, 16
	ds_read_b128 v[22:25], v56 offset:15360
	ds_read_b128 v[78:81], v73 offset:40960
	v_cvt_f16_f32_e32 v125, v33
	s_waitcnt vmcnt(6)
	v_cvt_f16_f32_e32 v126, v98
	v_cvt_pk_f16_f32 v127, v99, v100
	v_cvt_f16_f32_e32 v128, v101
	ds_read_b128 v[94:97], v56 offset:15424
	ds_read_b128 v[98:101], v73 offset:41024
	ds_read_b128 v[30:33], v56 offset:17920
	ds_read_b128 v[102:105], v56 offset:17984
	ds_read_b128 v[106:109], v56 offset:20480
	ds_read_b128 v[110:113], v56 offset:20544
	ds_write2st64_b64 v72, v[114:115], v[116:117] offset1:10
	global_load_dwordx4 v[114:117], v[60:61], off offset:1024
	v_pack_b32_f16 v124, v26, v57
	global_load_dwordx4 v[26:29], v[58:59], off offset:1024
	s_waitcnt lgkmcnt(0)
	v_mfma_f32_16x16x32_f16 v[74:77], v[22:25], v[78:81], v[74:77]
	ds_write2st64_b64 v72, v[118:119], v[120:121] offset0:20 offset1:60
	s_waitcnt vmcnt(7)
	v_cvt_f16_f32_e32 v42, v42
	v_cvt_f16_f32_e32 v45, v45
	v_mfma_f32_16x16x32_f16 v[82:85], v[30:33], v[78:81], v[82:85]
	ds_write_b64 v72, v[122:123] offset:35840
	s_waitcnt lgkmcnt(0)
	s_barrier
	global_load_dwordx4 v[22:25], v[66:67], off offset:1280
	global_load_dwordx4 v[30:33], v[64:65], off offset:1280
	v_cvt_pk_f16_f32 v43, v43, v44
	v_alignbit_b32 v125, v125, v57, 16
	v_mfma_f32_16x16x32_f16 v[50:53], v[106:109], v[78:81], v[50:53]
	v_pack_b32_f16 v108, v42, v43
	v_alignbit_b32 v109, v45, v43, 16
	s_waitcnt vmcnt(7)
	v_cvt_f16_f32_e32 v34, v34
	v_cvt_pk_f16_f32 v35, v35, v36
	v_cvt_f16_f32_e32 v36, v37
	v_mfma_f32_16x16x32_f16 v[42:45], v[94:97], v[98:101], v[74:77]
	v_cvt_f16_f32_e32 v57, v46
	s_waitcnt vmcnt(6)
	v_cvt_f16_f32_e32 v37, v41
	v_pack_b32_f16 v106, v126, v127
	v_cvt_f16_f32_e32 v74, v49
	v_cvt_pk_f16_f32 v75, v47, v48
	v_mfma_f32_16x16x32_f16 v[46:49], v[102:105], v[98:101], v[82:85]
	v_pack_b32_f16 v104, v34, v35
	v_cvt_f16_f32_e32 v34, v38
	v_alignbit_b32 v105, v36, v35, 16
	v_cvt_pk_f16_f32 v35, v39, v40
	v_alignbit_b32 v119, v37, v35, 16
	v_pack_b32_f16 v118, v34, v35
	ds_read_b128 v[34:37], v56
	v_pack_b32_f16 v102, v57, v75
	v_alignbit_b32 v103, v74, v75, 16
	ds_read_b128 v[74:77], v56 offset:2560
	ds_read_b128 v[78:81], v73 offset:30720
	s_waitcnt vmcnt(5)
	v_cvt_f16_f32_e32 v38, v90
	v_cvt_f16_f32_e32 v40, v93
	v_mfma_f32_16x16x32_f16 v[50:53], v[110:113], v[98:101], v[50:53]
	v_cvt_pk_f16_f32 v39, v91, v92
	v_pack_b32_f16 v120, v38, v39
	v_alignbit_b32 v121, v40, v39, 16
	ds_read_b128 v[82:85], v56 offset:5120
	ds_read_b128 v[90:93], v56 offset:64
	ds_read_b128 v[94:97], v73 offset:30784
	s_waitcnt lgkmcnt(3)
	v_mfma_f32_16x16x32_f16 v[34:37], v[34:37], v[78:81], v[42:45]
	global_load_dwordx4 v[38:41], v[62:63], off offset:1280
	v_alignbit_b32 v107, v128, v127, 16
	ds_read_b128 v[98:101], v56 offset:2624
	s_waitcnt vmcnt(5)
	v_cvt_f16_f32_e32 v42, v86
	v_cvt_f16_f32_e32 v44, v89
	v_mfma_f32_16x16x32_f16 v[74:77], v[74:77], v[78:81], v[46:49]
	v_cvt_pk_f16_f32 v43, v87, v88
	v_pack_b32_f16 v122, v42, v43
	v_alignbit_b32 v123, v44, v43, 16
	s_waitcnt lgkmcnt(3)
	v_mfma_f32_16x16x32_f16 v[78:81], v[82:85], v[78:81], v[50:53]
	global_load_dwordx4 v[42:45], v[58:59], off offset:1280
	ds_read_b128 v[86:89], v56 offset:5184
	ds_write2st64_b64 v72, v[124:125], v[106:107] offset0:30 offset1:40
	global_load_dwordx4 v[50:53], v[60:61], off offset:1280
	ds_write2st64_b64 v72, v[108:109], v[102:103] offset0:50 offset1:80
	ds_write_b64 v72, v[104:105] offset:46080
	s_waitcnt lgkmcnt(0)
	s_barrier
	global_load_dwordx4 v[46:49], v[66:67], off offset:1536
	global_load_dwordx4 v[82:85], v[64:65], off offset:1536
	v_mfma_f32_16x16x32_f16 v[78:81], v[86:89], v[94:97], v[78:81]
	ds_read_b128 v[86:89], v73 offset:40960
	s_waitcnt vmcnt(8)
	v_cvt_f16_f32_e32 v57, v114
	v_mfma_f32_16x16x32_f16 v[34:37], v[90:93], v[94:97], v[34:37]
	s_waitcnt vmcnt(7)
	v_cvt_f16_f32_e32 v26, v26
	v_cvt_f16_f32_e32 v29, v29
	v_cvt_pk_f16_f32 v27, v27, v28
	v_cvt_f16_f32_e32 v91, v117
	v_pack_b32_f16 v126, v26, v27
	v_alignbit_b32 v127, v29, v27, 16
	ds_read_b128 v[26:29], v56 offset:15360
	v_cvt_pk_f16_f32 v90, v115, v116
	v_pack_b32_f16 v124, v57, v90
	v_mfma_f32_16x16x32_f16 v[74:77], v[98:101], v[94:97], v[74:77]
	v_alignbit_b32 v125, v91, v90, 16
	s_waitcnt vmcnt(5)
	v_cvt_f16_f32_e32 v130, v30
	v_cvt_pk_f16_f32 v131, v31, v32
	v_cvt_f16_f32_e32 v132, v33
	ds_read_b128 v[90:93], v56 offset:15424
	global_load_dwordx4 v[94:97], v[62:63], off offset:1536
	ds_read_b128 v[98:101], v73 offset:41024
	s_waitcnt lgkmcnt(2)
	v_mfma_f32_16x16x32_f16 v[26:29], v[26:29], v[86:89], v[34:37]
	ds_read_b128 v[30:33], v56 offset:17920
	ds_read_b128 v[102:105], v56 offset:17984
	ds_read_b128 v[106:109], v56 offset:20480
	ds_read_b128 v[110:113], v56 offset:20544
	global_load_dwordx4 v[114:117], v[60:61], off offset:1536
	global_load_dwordx4 v[34:37], v[58:59], off offset:1536
	v_cvt_f16_f32_e32 v57, v22
	v_cvt_pk_f16_f32 v128, v23, v24
	v_cvt_f16_f32_e32 v129, v25
	ds_write2st64_b64 v72, v[118:119], v[120:121] offset1:10
	ds_write2st64_b64 v72, v[122:123], v[124:125] offset0:20 offset1:60
	ds_write_b64 v72, v[126:127] offset:35840
	s_waitcnt lgkmcnt(0)
	s_barrier
	global_load_dwordx4 v[22:25], v[66:67], off offset:1792
	v_mfma_f32_16x16x32_f16 v[74:77], v[30:33], v[86:89], v[74:77]
	global_load_dwordx4 v[30:33], v[64:65], off offset:1792
	v_pack_b32_f16 v118, v57, v128
	v_alignbit_b32 v119, v129, v128, 16
	v_mfma_f32_16x16x32_f16 v[64:67], v[106:109], v[86:89], v[78:81]
	v_pack_b32_f16 v120, v130, v131
	v_alignbit_b32 v121, v132, v131, 16
	s_waitcnt vmcnt(9)
	v_cvt_f16_f32_e32 v38, v38
	v_cvt_f16_f32_e32 v41, v41
	v_cvt_pk_f16_f32 v39, v39, v40
	v_mfma_f32_16x16x32_f16 v[78:81], v[90:93], v[98:101], v[26:29]
	v_pack_b32_f16 v106, v38, v39
	v_alignbit_b32 v107, v41, v39, 16
	s_waitcnt vmcnt(8)
	v_cvt_f16_f32_e32 v38, v42
	v_cvt_f16_f32_e32 v40, v45
	v_cvt_pk_f16_f32 v39, v43, v44
	s_waitcnt vmcnt(7)
	v_cvt_f16_f32_e32 v26, v50
	v_cvt_f16_f32_e32 v27, v53
	v_cvt_pk_f16_f32 v28, v51, v52
	v_mfma_f32_16x16x32_f16 v[50:53], v[102:105], v[98:101], v[74:77]
	v_pack_b32_f16 v102, v26, v28
	v_alignbit_b32 v103, v27, v28, 16
	global_load_dwordx4 v[26:29], v[62:63], off offset:1792
	v_pack_b32_f16 v104, v38, v39
	s_waitcnt vmcnt(7)
	v_cvt_f16_f32_e32 v38, v46
	v_alignbit_b32 v105, v40, v39, 16
	v_cvt_f16_f32_e32 v39, v49
	s_waitcnt vmcnt(6)
	v_cvt_f16_f32_e32 v44, v82
	v_cvt_pk_f16_f32 v40, v47, v48
	v_cvt_pk_f16_f32 v48, v83, v84
	v_pack_b32_f16 v38, v38, v40
	v_alignbit_b32 v39, v39, v40, 16
	ds_read_b128 v[40:43], v56
	v_pack_b32_f16 v108, v44, v48
	v_cvt_f16_f32_e32 v49, v85
	ds_read_b128 v[44:47], v56 offset:2560
	ds_read_b128 v[74:77], v73 offset:30720
	ds_read_b128 v[82:85], v56 offset:5120
	global_load_dwordx4 v[60:63], v[60:61], off offset:1792
	v_mfma_f32_16x16x32_f16 v[64:67], v[110:113], v[98:101], v[64:67]
	ds_read_b128 v[86:89], v56 offset:64
	ds_read_b128 v[90:93], v73 offset:30784
	global_load_dwordx4 v[98:101], v[58:59], off offset:1792
	v_alignbit_b32 v109, v49, v48, 16
	s_waitcnt lgkmcnt(3)
	v_mfma_f32_16x16x32_f16 v[40:43], v[40:43], v[74:77], v[78:81]
	s_waitcnt vmcnt(7)
	v_cvt_pk_f16_f32 v57, v95, v96
	s_nop 0
	ds_read_b128 v[78:81], v56 offset:2624
	v_mfma_f32_16x16x32_f16 v[44:47], v[44:47], v[74:77], v[50:53]
	s_waitcnt vmcnt(6)
	v_cvt_f16_f32_e32 v59, v117
	s_waitcnt vmcnt(5)
	v_cvt_f16_f32_e32 v34, v34
	ds_read_b128 v[48:51], v56 offset:5184
	v_cvt_f16_f32_e32 v52, v94
	v_cvt_f16_f32_e32 v53, v97
	v_cvt_f16_f32_e32 v37, v37
	v_cvt_pk_f16_f32 v35, v35, v36
	s_waitcnt lgkmcnt(4)
	v_mfma_f32_16x16x32_f16 v[64:67], v[82:85], v[74:77], v[64:67]
	v_pack_b32_f16 v52, v52, v57
	v_alignbit_b32 v53, v53, v57, 16
	v_cvt_f16_f32_e32 v57, v114
	s_waitcnt lgkmcnt(2)
	v_mfma_f32_16x16x32_f16 v[40:43], v[86:89], v[90:93], v[40:43]
	ds_write2st64_b64 v72, v[118:119], v[120:121] offset0:30 offset1:40
	ds_write2st64_b64 v72, v[106:107], v[102:103] offset0:50 offset1:80
	ds_write_b64 v72, v[104:105] offset:46080
	v_pack_b32_f16 v86, v34, v35
	v_alignbit_b32 v87, v37, v35, 16
	s_waitcnt lgkmcnt(0)
	s_barrier
	ds_read_b128 v[34:37], v56 offset:15360
	v_cvt_pk_f16_f32 v74, v115, v116
	v_pack_b32_f16 v58, v57, v74
	v_alignbit_b32 v59, v59, v74, 16
	v_mfma_f32_16x16x32_f16 v[48:51], v[48:51], v[90:93], v[64:67]
	s_nop 2
	ds_read_b128 v[64:67], v56 offset:17920
	ds_read_b128 v[74:77], v73 offset:40960
	s_waitcnt vmcnt(4)
	v_cvt_f16_f32_e32 v57, v22
	v_cvt_pk_f16_f32 v89, v23, v24
	v_mfma_f32_16x16x32_f16 v[44:47], v[78:81], v[90:93], v[44:47]
	v_cvt_f16_f32_e32 v90, v25
	ds_read_b128 v[22:25], v56 offset:20480
	ds_read_b128 v[78:81], v56 offset:15424
	ds_read_b128 v[82:85], v73 offset:41024
	s_waitcnt vmcnt(3)
	v_cvt_f16_f32_e32 v30, v30
	s_waitcnt lgkmcnt(3)
	v_mfma_f32_16x16x32_f16 v[34:37], v[34:37], v[74:77], v[40:43]
	v_cvt_f16_f32_e32 v33, v33
	v_cvt_pk_f16_f32 v31, v31, v32
	v_pack_b32_f16 v88, v57, v89
	ds_read_b128 v[40:43], v56 offset:17984
	v_mfma_f32_16x16x32_f16 v[44:47], v[64:67], v[74:77], v[44:47]
	ds_read_b128 v[64:67], v56 offset:20544
	v_alignbit_b32 v89, v90, v89, 16
	v_pack_b32_f16 v90, v30, v31
	s_waitcnt lgkmcnt(4)
	v_mfma_f32_16x16x32_f16 v[22:25], v[22:25], v[74:77], v[48:51]
	v_alignbit_b32 v91, v33, v31, 16
	ds_write2st64_b64 v72, v[38:39], v[108:109] offset1:10
	ds_write2st64_b64 v72, v[52:53], v[58:59] offset0:20 offset1:60
	ds_write_b64 v72, v[86:87] offset:35840
	s_waitcnt lgkmcnt(0)
	v_mfma_f32_16x16x32_f16 v[30:33], v[78:81], v[82:85], v[34:37]
	s_barrier
	s_waitcnt vmcnt(2)
	v_cvt_f16_f32_e32 v57, v26
	ds_read_b128 v[34:37], v56
	v_mfma_f32_16x16x32_f16 v[38:41], v[40:43], v[82:85], v[44:47]
	s_nop 2
	ds_read_b128 v[42:45], v56 offset:2560
	ds_read_b128 v[46:49], v73 offset:30720
	v_cvt_pk_f16_f32 v58, v27, v28
	v_cvt_f16_f32_e32 v59, v29
	v_mfma_f32_16x16x32_f16 v[22:25], v[64:67], v[82:85], v[22:25]
	ds_read_b128 v[50:53], v56 offset:5120
	ds_read_b128 v[64:67], v56 offset:64
	ds_read_b128 v[74:77], v73 offset:30784
	ds_read_b128 v[26:29], v56 offset:2624
	s_waitcnt lgkmcnt(4)
	v_mfma_f32_16x16x32_f16 v[30:33], v[34:37], v[46:49], v[30:33]
	v_mfma_f32_16x16x32_f16 v[34:37], v[42:45], v[46:49], v[38:41]
	s_waitcnt vmcnt(1)
	v_cvt_f16_f32_e32 v44, v60
	v_cvt_f16_f32_e32 v45, v63
	v_pack_b32_f16 v42, v57, v58
	s_waitcnt lgkmcnt(3)
	v_mfma_f32_16x16x32_f16 v[22:25], v[50:53], v[46:49], v[22:25]
	v_cvt_pk_f16_f32 v46, v61, v62
	ds_read_b128 v[38:41], v56 offset:5184
	v_pack_b32_f16 v44, v44, v46
	v_alignbit_b32 v45, v45, v46, 16
	s_waitcnt vmcnt(0)
	v_cvt_f16_f32_e32 v46, v98
	s_waitcnt lgkmcnt(1)
	v_mfma_f32_16x16x32_f16 v[26:29], v[26:29], v[74:77], v[34:37]
	v_alignbit_b32 v43, v59, v58, 16
	ds_write2st64_b64 v72, v[88:89], v[90:91] offset0:30 offset1:40
	ds_write2st64_b64 v72, v[42:43], v[44:45] offset0:50 offset1:80
	v_cvt_f16_f32_e32 v35, v101
	v_cvt_pk_f16_f32 v36, v99, v100
	v_pack_b32_f16 v34, v46, v36
	v_mfma_f32_16x16x32_f16 v[30:33], v[64:67], v[74:77], v[30:33]
	v_alignbit_b32 v35, v35, v36, 16
	ds_write_b64 v72, v[34:35] offset:46080
	s_waitcnt lgkmcnt(0)
	s_barrier
	ds_read_b128 v[34:37], v56 offset:15360
	v_mfma_f32_16x16x32_f16 v[22:25], v[38:41], v[74:77], v[22:25]
	ds_read_b128 v[38:41], v73 offset:40960
	ds_read_b128 v[42:45], v56 offset:15424
	ds_read_b128 v[46:49], v73 offset:41024
	s_waitcnt lgkmcnt(2)
	v_mfma_f32_16x16x32_f16 v[30:33], v[34:37], v[38:41], v[30:33]
	ds_read_b128 v[34:37], v56 offset:17920
	ds_read_b128 v[50:53], v56 offset:17984
	s_waitcnt lgkmcnt(2)
	v_mfma_f32_16x16x32_f16 v[30:33], v[42:45], v[46:49], v[30:33]
	s_waitcnt lgkmcnt(1)
	v_mfma_f32_16x16x32_f16 v[26:29], v[34:37], v[38:41], v[26:29]
	ds_read_b128 v[34:37], v56 offset:20480
	ds_read_b128 v[56:59], v56 offset:20544
	s_waitcnt vmcnt(0)
	s_waitcnt lgkmcnt(0)
	s_nop 2
	v_add_f32_e32 v2, v30, v69
	v_mfma_f32_16x16x32_f16 v[26:29], v[50:53], v[46:49], v[26:29]
	v_cvt_f16_f32_e32 v2, v2
	v_add_f32_e32 v3, v31, v69
	v_cvt_f16_f32_e32 v3, v3
	v_mfma_f32_16x16x32_f16 v[22:25], v[34:37], v[38:41], v[22:25]
	v_add_f32_e32 v4, v32, v69
	v_cvt_f16_f32_e32 v4, v4
	v_add_f32_e32 v5, v33, v69
	v_cvt_f16_f32_e32 v5, v5
	s_barrier
	ds_write_b16 v1, v2
	ds_write_b16 v1, v3 offset:160
	ds_write_b16 v1, v4 offset:320
	ds_write_b16 v1, v5 offset:480
	v_add_f32_e32 v2, v26, v69
	v_mfma_f32_16x16x32_f16 v[22:25], v[56:59], v[46:49], v[22:25]
	v_cvt_f16_f32_e32 v2, v2
	v_add_f32_e32 v3, v27, v69
	v_cvt_f16_f32_e32 v3, v3
	v_add_f32_e32 v4, v28, v69
	v_cvt_f16_f32_e32 v4, v4
	v_add_f32_e32 v5, v29, v69
	v_cvt_f16_f32_e32 v5, v5
	ds_write_b16 v1, v2 offset:2560
	ds_write_b16 v1, v3 offset:2720
	ds_write_b16 v1, v4 offset:2880
	ds_write_b16 v1, v5 offset:3040
	v_add_f32_e32 v2, v22, v69
	v_cvt_f16_f32_e32 v2, v2
	v_add_f32_e32 v3, v23, v69
	v_cvt_f16_f32_e32 v3, v3
	v_add_f32_e32 v4, v24, v69
	v_cvt_f16_f32_e32 v4, v4
	v_add_f32_e32 v5, v25, v69
	v_cvt_f16_f32_e32 v5, v5
	ds_write_b16 v1, v2 offset:5120
	ds_write_b16 v1, v3 offset:5280
	ds_write_b16 v1, v4 offset:5440
	ds_write_b16 v1, v5 offset:5600
	v_and_b32_e32 v2, 7, v0
	v_mul_u32_u24_e32 v10, 12, v2
	v_mul_u32_u24_e32 v2, 0x3c0, v2
	v_lshrrev_b32_e32 v1, 3, v0
	v_lshlrev_b32_e32 v2, 1, v2
	v_lshl_add_u32 v3, v1, 1, v2
	s_waitcnt lgkmcnt(0)
	s_barrier
	ds_read_u16 v2, v3
	ds_read_u16 v4, v3 offset:160
	ds_read_u16 v5, v3 offset:320
	ds_read_u16 v6, v3 offset:480
	ds_read_u16 v7, v3 offset:640
	ds_read_u16 v8, v3 offset:800
	ds_read_u16 v9, v3 offset:960
	ds_read_u16 v11, v3 offset:1120
	ds_read_u16 v12, v3 offset:1280
	ds_read_u16 v13, v3 offset:1440
	ds_read_u16 v14, v3 offset:1600
	ds_read_u16 v15, v3 offset:1760
	v_lshl_or_b32 v1, s18, 9, v1
	s_waitcnt lgkmcnt(10)
	v_lshl_or_b32 v2, v4, 16, v2
	s_waitcnt lgkmcnt(6)
	v_lshl_or_b32 v4, v8, 16, v7
	v_or_b32_e32 v1, s20, v1
	v_mov_b32_e32 v8, s19
	v_mad_u32_u24 v54, v1, s15, v8
	v_lshl_or_b32 v3, v6, 16, v5
	s_waitcnt lgkmcnt(4)
	v_lshl_or_b32 v5, v11, 16, v9
	v_lshl_add_u64 v[8:9], v[54:55], 1, s[12:13]
	v_lshlrev_b32_e32 v54, 1, v10
	v_lshl_add_u64 v[8:9], v[8:9], 0, v[54:55]
	s_waitcnt lgkmcnt(2)
	v_lshl_or_b32 v6, v13, 16, v12
	s_waitcnt lgkmcnt(0)
	v_lshl_or_b32 v7, v15, 16, v14
	global_store_dwordx4 v[8:9], v[2:5], off
	global_store_dwordx2 v[8:9], v[6:7], off offset:16
	s_mov_b64 s[12:13], 0
